# csr layer-1 gather rewritten: 8 lanes per node with 16-byte loads, all 64 nodes of a bucket in one round (half the load instructions)
# speedup vs baseline: 1.1077x; 1.0345x over previous
.LBB1_129:
	s_ashr_i32 s11, s10, 31
	s_lshl_b64 s[2:3], s[10:11], 1
	s_add_u32 s4, s28, s2
	s_addc_u32 s5, s29, s3
	v_add_u32_e32 v46, s14, v38
	s_mov_b32 s10, 0
	s_mov_b64 s[6:7], -1
	s_mov_b32 s14, 0xc350
	v_lshlrev_b32_e32 v47, 3, v44
	v_mov_b32_e32 v48, 0x4000
	s_and_b64 vcc, exec, s[0:1]
	s_cbranch_vccz .Lg4_start
	s_branch .LBB1_134

.Lg4_start:
	v_lshl_or_b32 v60, v38, 4, v44
	v_lshrrev_b32_e32 v62, 3, v60
	v_and_b32_e32 v61, 7, v60
	v_lshlrev_b32_e32 v61, 4, v61
	v_lshlrev_b32_e32 v63, 2, v38
	v_sub_u32_e32 v58, v45, v63
	v_lshl_add_u32 v58, v62, 2, v58
	v_sub_u32_e32 v60, v46, v38
	v_add_u32_e32 v60, v60, v62
	v_cmp_gt_i32_e32 vcc, s14, v60
	s_and_saveexec_b64 s[8:9], vcc
	s_cbranch_execz .Lg4_end
	ds_read2_b32 v[56:57], v58 offset1:1
	v_mov_b32_e32 v0, 0
	v_mov_b32_e32 v1, 0
	v_mov_b32_e32 v2, 0
	v_mov_b32_e32 v3, 0
	v_mov_b32_e32 v4, 0
	v_mov_b32_e32 v5, 0
	v_mov_b32_e32 v6, 0
	v_mov_b32_e32 v7, 0
	v_mov_b32_e32 v8, 0
	v_mov_b32_e32 v9, 0
	v_mov_b32_e32 v10, 0
	v_mov_b32_e32 v11, 0
	v_mov_b32_e32 v12, 0
	v_mov_b32_e32 v13, 0
	v_mov_b32_e32 v14, 0
	v_mov_b32_e32 v15, 0
	v_mov_b32_e32 v63, 0xc378
	s_waitcnt lgkmcnt(0)
	v_sub_u32_e32 v59, v57, v56
	v_lshlrev_b32_e32 v58, 1, v56
	v_add_u32_e32 v58, 0x4000, v58
	v_cmp_lt_i32_e32 vcc, 0, v59
	s_and_saveexec_b64 s[10:11], vcc
	s_cbranch_execz .Lg4_loop_skip
	s_mov_b32 s15, 0
	s_mov_b64 s[2:3], 0
.Lg4_loop:
	ds_read_u16 v48, v58
	ds_read_u16 v49, v58 offset:2
	ds_read_u16 v50, v58 offset:4
	ds_read_u16 v51, v58 offset:6
	ds_read_u16 v52, v58 offset:8
	ds_read_u16 v53, v58 offset:10
	ds_read_u16 v54, v58 offset:12
	ds_read_u16 v55, v58 offset:14
	s_add_i32 s12, s15, 1
	v_cmp_lt_i32_e64 s[46:47], s12, v59
	s_add_i32 s12, s15, 2
	v_cmp_lt_i32_e64 s[48:49], s12, v59
	s_add_i32 s12, s15, 3
	v_cmp_lt_i32_e64 s[50:51], s12, v59
	s_add_i32 s12, s15, 4
	v_cmp_lt_i32_e64 s[52:53], s12, v59
	s_add_i32 s12, s15, 5
	v_cmp_lt_i32_e64 s[54:55], s12, v59
	s_add_i32 s12, s15, 6
	v_cmp_lt_i32_e64 s[56:57], s12, v59
	s_add_i32 s12, s15, 7
	v_cmp_lt_i32_e64 s[58:59], s12, v59
	s_waitcnt lgkmcnt(7)
	v_lshl_or_b32 v48, v48, 7, v61
	global_load_dwordx4 v[16:19], v48, s[34:35]
	s_waitcnt lgkmcnt(6)
	v_cndmask_b32_e64 v49, v63, v49, s[46:47]
	v_lshl_or_b32 v49, v49, 7, v61
	global_load_dwordx4 v[20:23], v49, s[34:35]
	s_waitcnt lgkmcnt(5)
	v_cndmask_b32_e64 v50, v63, v50, s[48:49]
	v_lshl_or_b32 v50, v50, 7, v61
	global_load_dwordx4 v[24:27], v50, s[34:35]
	s_waitcnt lgkmcnt(4)
	v_cndmask_b32_e64 v51, v63, v51, s[50:51]
	v_lshl_or_b32 v51, v51, 7, v61
	global_load_dwordx4 v[28:31], v51, s[34:35]
	s_waitcnt lgkmcnt(3)
	v_cndmask_b32_e64 v52, v63, v52, s[52:53]
	v_lshl_or_b32 v52, v52, 7, v61
	global_load_dwordx4 v[32:35], v52, s[34:35]
	s_waitcnt lgkmcnt(2)
	v_cndmask_b32_e64 v53, v63, v53, s[54:55]
	v_lshl_or_b32 v53, v53, 7, v61
	global_load_dwordx4 v[36:39], v53, s[34:35]
	s_waitcnt lgkmcnt(1)
	v_cndmask_b32_e64 v54, v63, v54, s[56:57]
	v_lshl_or_b32 v54, v54, 7, v61
	global_load_dwordx4 v[40:43], v54, s[34:35]
	s_waitcnt lgkmcnt(0)
	v_cndmask_b32_e64 v55, v63, v55, s[58:59]
	v_lshl_or_b32 v55, v55, 7, v61
	global_load_dwordx4 v[44:47], v55, s[34:35]
	s_waitcnt vmcnt(7)
	v_cvt_pk_f32_fp8_e32 v[48:49], v16
	v_cvt_pk_f32_fp8_sdwa v[50:51], v16 src0_sel:WORD_1
	v_pk_add_f32 v[0:1], v[0:1], v[48:49]
	v_pk_add_f32 v[2:3], v[2:3], v[50:51]
	v_cvt_pk_f32_fp8_e32 v[52:53], v17
	v_cvt_pk_f32_fp8_sdwa v[54:55], v17 src0_sel:WORD_1
	v_pk_add_f32 v[4:5], v[4:5], v[52:53]
	v_pk_add_f32 v[6:7], v[6:7], v[54:55]
	v_cvt_pk_f32_fp8_e32 v[48:49], v18
	v_cvt_pk_f32_fp8_sdwa v[50:51], v18 src0_sel:WORD_1
	v_pk_add_f32 v[8:9], v[8:9], v[48:49]
	v_pk_add_f32 v[10:11], v[10:11], v[50:51]
	v_cvt_pk_f32_fp8_e32 v[52:53], v19
	v_cvt_pk_f32_fp8_sdwa v[54:55], v19 src0_sel:WORD_1
	v_pk_add_f32 v[12:13], v[12:13], v[52:53]
	v_pk_add_f32 v[14:15], v[14:15], v[54:55]
	s_waitcnt vmcnt(6)
	v_cvt_pk_f32_fp8_e32 v[48:49], v20
	v_cvt_pk_f32_fp8_sdwa v[50:51], v20 src0_sel:WORD_1
	v_pk_add_f32 v[0:1], v[0:1], v[48:49]
	v_pk_add_f32 v[2:3], v[2:3], v[50:51]
	v_cvt_pk_f32_fp8_e32 v[52:53], v21
	v_cvt_pk_f32_fp8_sdwa v[54:55], v21 src0_sel:WORD_1
	v_pk_add_f32 v[4:5], v[4:5], v[52:53]
	v_pk_add_f32 v[6:7], v[6:7], v[54:55]
	v_cvt_pk_f32_fp8_e32 v[48:49], v22
	v_cvt_pk_f32_fp8_sdwa v[50:51], v22 src0_sel:WORD_1
	v_pk_add_f32 v[8:9], v[8:9], v[48:49]
	v_pk_add_f32 v[10:11], v[10:11], v[50:51]
	v_cvt_pk_f32_fp8_e32 v[52:53], v23
	v_cvt_pk_f32_fp8_sdwa v[54:55], v23 src0_sel:WORD_1
	v_pk_add_f32 v[12:13], v[12:13], v[52:53]
	v_pk_add_f32 v[14:15], v[14:15], v[54:55]
	s_waitcnt vmcnt(5)
	v_cvt_pk_f32_fp8_e32 v[48:49], v24
	v_cvt_pk_f32_fp8_sdwa v[50:51], v24 src0_sel:WORD_1
	v_pk_add_f32 v[0:1], v[0:1], v[48:49]
	v_pk_add_f32 v[2:3], v[2:3], v[50:51]
	v_cvt_pk_f32_fp8_e32 v[52:53], v25
	v_cvt_pk_f32_fp8_sdwa v[54:55], v25 src0_sel:WORD_1
	v_pk_add_f32 v[4:5], v[4:5], v[52:53]
	v_pk_add_f32 v[6:7], v[6:7], v[54:55]
	v_cvt_pk_f32_fp8_e32 v[48:49], v26
	v_cvt_pk_f32_fp8_sdwa v[50:51], v26 src0_sel:WORD_1
	v_pk_add_f32 v[8:9], v[8:9], v[48:49]
	v_pk_add_f32 v[10:11], v[10:11], v[50:51]
	v_cvt_pk_f32_fp8_e32 v[52:53], v27
	v_cvt_pk_f32_fp8_sdwa v[54:55], v27 src0_sel:WORD_1
	v_pk_add_f32 v[12:13], v[12:13], v[52:53]
	v_pk_add_f32 v[14:15], v[14:15], v[54:55]
	s_waitcnt vmcnt(4)
	v_cvt_pk_f32_fp8_e32 v[48:49], v28
	v_cvt_pk_f32_fp8_sdwa v[50:51], v28 src0_sel:WORD_1
	v_pk_add_f32 v[0:1], v[0:1], v[48:49]
	v_pk_add_f32 v[2:3], v[2:3], v[50:51]
	v_cvt_pk_f32_fp8_e32 v[52:53], v29
	v_cvt_pk_f32_fp8_sdwa v[54:55], v29 src0_sel:WORD_1
	v_pk_add_f32 v[4:5], v[4:5], v[52:53]
	v_pk_add_f32 v[6:7], v[6:7], v[54:55]
	v_cvt_pk_f32_fp8_e32 v[48:49], v30
	v_cvt_pk_f32_fp8_sdwa v[50:51], v30 src0_sel:WORD_1
	v_pk_add_f32 v[8:9], v[8:9], v[48:49]
	v_pk_add_f32 v[10:11], v[10:11], v[50:51]
	v_cvt_pk_f32_fp8_e32 v[52:53], v31
	v_cvt_pk_f32_fp8_sdwa v[54:55], v31 src0_sel:WORD_1
	v_pk_add_f32 v[12:13], v[12:13], v[52:53]
	v_pk_add_f32 v[14:15], v[14:15], v[54:55]
	s_waitcnt vmcnt(3)
	v_cvt_pk_f32_fp8_e32 v[48:49], v32
	v_cvt_pk_f32_fp8_sdwa v[50:51], v32 src0_sel:WORD_1
	v_pk_add_f32 v[0:1], v[0:1], v[48:49]
	v_pk_add_f32 v[2:3], v[2:3], v[50:51]
	v_cvt_pk_f32_fp8_e32 v[52:53], v33
	v_cvt_pk_f32_fp8_sdwa v[54:55], v33 src0_sel:WORD_1
	v_pk_add_f32 v[4:5], v[4:5], v[52:53]
	v_pk_add_f32 v[6:7], v[6:7], v[54:55]
	v_cvt_pk_f32_fp8_e32 v[48:49], v34
	v_cvt_pk_f32_fp8_sdwa v[50:51], v34 src0_sel:WORD_1
	v_pk_add_f32 v[8:9], v[8:9], v[48:49]
	v_pk_add_f32 v[10:11], v[10:11], v[50:51]
	v_cvt_pk_f32_fp8_e32 v[52:53], v35
	v_cvt_pk_f32_fp8_sdwa v[54:55], v35 src0_sel:WORD_1
	v_pk_add_f32 v[12:13], v[12:13], v[52:53]
	v_pk_add_f32 v[14:15], v[14:15], v[54:55]
	s_waitcnt vmcnt(2)
	v_cvt_pk_f32_fp8_e32 v[48:49], v36
	v_cvt_pk_f32_fp8_sdwa v[50:51], v36 src0_sel:WORD_1
	v_pk_add_f32 v[0:1], v[0:1], v[48:49]
	v_pk_add_f32 v[2:3], v[2:3], v[50:51]
	v_cvt_pk_f32_fp8_e32 v[52:53], v37
	v_cvt_pk_f32_fp8_sdwa v[54:55], v37 src0_sel:WORD_1
	v_pk_add_f32 v[4:5], v[4:5], v[52:53]
	v_pk_add_f32 v[6:7], v[6:7], v[54:55]
	v_cvt_pk_f32_fp8_e32 v[48:49], v38
	v_cvt_pk_f32_fp8_sdwa v[50:51], v38 src0_sel:WORD_1
	v_pk_add_f32 v[8:9], v[8:9], v[48:49]
	v_pk_add_f32 v[10:11], v[10:11], v[50:51]
	v_cvt_pk_f32_fp8_e32 v[52:53], v39
	v_cvt_pk_f32_fp8_sdwa v[54:55], v39 src0_sel:WORD_1
	v_pk_add_f32 v[12:13], v[12:13], v[52:53]
	v_pk_add_f32 v[14:15], v[14:15], v[54:55]
	s_waitcnt vmcnt(1)
	v_cvt_pk_f32_fp8_e32 v[48:49], v40
	v_cvt_pk_f32_fp8_sdwa v[50:51], v40 src0_sel:WORD_1
	v_pk_add_f32 v[0:1], v[0:1], v[48:49]
	v_pk_add_f32 v[2:3], v[2:3], v[50:51]
	v_cvt_pk_f32_fp8_e32 v[52:53], v41
	v_cvt_pk_f32_fp8_sdwa v[54:55], v41 src0_sel:WORD_1
	v_pk_add_f32 v[4:5], v[4:5], v[52:53]
	v_pk_add_f32 v[6:7], v[6:7], v[54:55]
	v_cvt_pk_f32_fp8_e32 v[48:49], v42
	v_cvt_pk_f32_fp8_sdwa v[50:51], v42 src0_sel:WORD_1
	v_pk_add_f32 v[8:9], v[8:9], v[48:49]
	v_pk_add_f32 v[10:11], v[10:11], v[50:51]
	v_cvt_pk_f32_fp8_e32 v[52:53], v43
	v_cvt_pk_f32_fp8_sdwa v[54:55], v43 src0_sel:WORD_1
	v_pk_add_f32 v[12:13], v[12:13], v[52:53]
	v_pk_add_f32 v[14:15], v[14:15], v[54:55]
	s_waitcnt vmcnt(0)
	v_cvt_pk_f32_fp8_e32 v[48:49], v44
	v_cvt_pk_f32_fp8_sdwa v[50:51], v44 src0_sel:WORD_1
	v_pk_add_f32 v[0:1], v[0:1], v[48:49]
	v_pk_add_f32 v[2:3], v[2:3], v[50:51]
	v_cvt_pk_f32_fp8_e32 v[52:53], v45
	v_cvt_pk_f32_fp8_sdwa v[54:55], v45 src0_sel:WORD_1
	v_pk_add_f32 v[4:5], v[4:5], v[52:53]
	v_pk_add_f32 v[6:7], v[6:7], v[54:55]
	v_cvt_pk_f32_fp8_e32 v[48:49], v46
	v_cvt_pk_f32_fp8_sdwa v[50:51], v46 src0_sel:WORD_1
	v_pk_add_f32 v[8:9], v[8:9], v[48:49]
	v_pk_add_f32 v[10:11], v[10:11], v[50:51]
	v_cvt_pk_f32_fp8_e32 v[52:53], v47
	v_cvt_pk_f32_fp8_sdwa v[54:55], v47 src0_sel:WORD_1
	v_pk_add_f32 v[12:13], v[12:13], v[52:53]
	v_pk_add_f32 v[14:15], v[14:15], v[54:55]
	s_add_i32 s15, s15, 8
	v_cmp_ge_i32_e32 vcc, s15, v59
	v_add_u32_e32 v58, 16, v58
	s_or_b64 s[2:3], vcc, s[2:3]
	s_andn2_b64 exec, exec, s[2:3]
	s_cbranch_execnz .Lg4_loop
.Lg4_loop_skip:
	s_or_b64 exec, exec, s[10:11]
	v_cvt_f32_i32_e32 v48, v59
	v_max_f32_e32 v48, 1.0, v48
	v_rcp_f32_e32 v48, v48
	v_lshl_or_b32 v20, v60, 7, v61
	v_mul_f32_e32 v0, v0, v48
	v_mul_f32_e32 v1, v1, v48
	v_mul_f32_e32 v2, v2, v48
	v_mul_f32_e32 v3, v3, v48
	v_mul_f32_e32 v4, v4, v48
	v_mul_f32_e32 v5, v5, v48
	v_mul_f32_e32 v6, v6, v48
	v_mul_f32_e32 v7, v7, v48
	v_mul_f32_e32 v8, v8, v48
	v_mul_f32_e32 v9, v9, v48
	v_mul_f32_e32 v10, v10, v48
	v_mul_f32_e32 v11, v11, v48
	v_mul_f32_e32 v12, v12, v48
	v_mul_f32_e32 v13, v13, v48
	v_mul_f32_e32 v14, v14, v48
	v_mul_f32_e32 v15, v15, v48
	v_cvt_pk_fp8_f32 v16, v0, v1
	v_cvt_pk_fp8_f32 v17, v4, v5
	v_cvt_pk_fp8_f32 v18, v8, v9
	v_cvt_pk_fp8_f32 v19, v12, v13
	v_cvt_pk_fp8_f32 v16, v2, v3 op_sel:[0,0,1]
	v_cvt_pk_fp8_f32 v17, v6, v7 op_sel:[0,0,1]
	v_cvt_pk_fp8_f32 v18, v10, v11 op_sel:[0,0,1]
	v_cvt_pk_fp8_f32 v19, v14, v15 op_sel:[0,0,1]
	s_nop 0
	global_store_dwordx4 v20, v[16:19], s[36:37] nt

	.amdhsa_kernel _Z10k_csr_agg1PKjPKiPiPtPjPK15HIP_vector_typeIjLj2EEPS7_SA_
		.amdhsa_group_segment_fixed_size 25136
		.amdhsa_private_segment_fixed_size 0
		.amdhsa_kernarg_size 64
		.amdhsa_user_sgpr_count 2
		.amdhsa_user_sgpr_dispatch_ptr 0
		.amdhsa_user_sgpr_queue_ptr 0
		.amdhsa_user_sgpr_kernarg_segment_ptr 1
		.amdhsa_user_sgpr_dispatch_id 0
		.amdhsa_user_sgpr_kernarg_preload_length 0
		.amdhsa_user_sgpr_kernarg_preload_offset 0
		.amdhsa_user_sgpr_private_segment_size 0
		.amdhsa_uses_dynamic_stack 0
		.amdhsa_enable_private_segment 0
		.amdhsa_system_sgpr_workgroup_id_x 1
		.amdhsa_system_sgpr_workgroup_id_y 0
		.amdhsa_system_sgpr_workgroup_id_z 0
		.amdhsa_system_sgpr_workgroup_info 0
		.amdhsa_system_vgpr_workitem_id 0
		.amdhsa_next_free_vgpr 64
		.amdhsa_next_free_sgpr 60
		.amdhsa_accum_offset 64
		.amdhsa_reserve_vcc 1
		.amdhsa_float_round_mode_32 0
		.amdhsa_float_round_mode_16_64 0
		.amdhsa_float_denorm_mode_32 3
		.amdhsa_float_denorm_mode_16_64 3
		.amdhsa_dx10_clamp 1
		.amdhsa_ieee_mode 1
		.amdhsa_fp16_overflow 0
		.amdhsa_tg_split 0
		.amdhsa_exception_fp_ieee_invalid_op 0
		.amdhsa_exception_fp_denorm_src 0
		.amdhsa_exception_fp_ieee_div_zero 0
		.amdhsa_exception_fp_ieee_overflow 0
		.amdhsa_exception_fp_ieee_underflow 0
		.amdhsa_exception_fp_ieee_inexact 0
		.amdhsa_exception_int_div_zero 0
	.end_amdhsa_kernel
